# speedup vs baseline: 1.0220x; 1.0220x over previous
.LBB3_20:
	s_or_b64 exec, exec, s[6:7]
	v_mul_u32_u24_e32 v2, 0x25f, v0
	s_load_dwordx2 s[12:13], s[0:1], 0x30
	v_lshrrev_b32_e32 v2, 16, v2
	s_movk_i32 s1, 0xff94
	v_mad_i32_i24 v3, v2, s1, v0
	v_mul_i32_i24_e32 v4, 0xe39, v3
	v_lshrrev_b32_e32 v5, 31, v4
	v_add_u16_sdwa v4, v4, v5 dst_sel:DWORD dst_unused:UNUSED_PAD src0_sel:WORD_1 src1_sel:DWORD
	v_bfe_i32 v4, v4, 0, 16
	s_movk_i32 s7, 0xffee
	s_add_i32 s0, s22, -4
	v_mad_i32_i24 v3, v4, s7, v3
	v_add_u32_e32 v4, s25, v4
	v_mov_b32_e32 v5, 0x7f
	v_med3_i32 v4, v4, 0, v5
	v_lshl_add_u32 v3, v3, 2, s0
	v_mov_b32_e32 v6, 0x7c
	v_med3_i32 v3, v3, 0, v6
	v_lshlrev_b32_e32 v2, 14, v2
	v_lshlrev_b32_e32 v4, 7, v4
	v_or3_b32 v94, v4, v2, v3
	v_lshl_or_b32 v2, v49, 6, v1
	v_mul_u32_u24_e32 v3, 0x25f, v2
	v_lshrrev_b32_e32 v3, 16, v3
	s_movk_i32 s6, 0xe39
	v_mad_i32_i24 v2, v3, s1, v2
	v_mul_i32_i24_sdwa v4, sext(v2), s6 dst_sel:DWORD dst_unused:UNUSED_PAD src0_sel:WORD_0 src1_sel:DWORD
	v_lshrrev_b32_e32 v7, 31, v4
	v_add_u16_sdwa v4, v4, v7 dst_sel:DWORD dst_unused:UNUSED_PAD src0_sel:WORD_1 src1_sel:DWORD
	v_bfe_i32 v4, v4, 0, 16
	v_mad_i32_i24 v2, v4, s7, v2
	v_add_u32_e32 v4, s25, v4
	v_med3_i32 v4, v4, 0, v5
	v_lshl_add_u32 v2, v2, 2, s0
	v_med3_i32 v2, v2, 0, v6
	v_lshlrev_b32_e32 v3, 14, v3
	v_lshlrev_b32_e32 v4, 7, v4
	v_min_u32_e32 v47, 27, v50
	v_or3_b32 v96, v4, v3, v2
	v_lshl_or_b32 v2, v47, 6, v1
	v_mul_u32_u24_e32 v3, 0x25f, v2
	v_lshrrev_b32_e32 v3, 16, v3
	v_mad_i32_i24 v2, v3, s1, v2
	v_mul_i32_i24_sdwa v4, sext(v2), s6 dst_sel:DWORD dst_unused:UNUSED_PAD src0_sel:WORD_0 src1_sel:DWORD
	v_lshrrev_b32_e32 v7, 31, v4
	v_add_u16_sdwa v4, v4, v7 dst_sel:DWORD dst_unused:UNUSED_PAD src0_sel:WORD_1 src1_sel:DWORD
	v_bfe_i32 v4, v4, 0, 16
	v_mad_i32_i24 v2, v4, s7, v2
	v_add_u32_e32 v4, s25, v4
	v_min_u32_e32 v3, 15, v3
	v_med3_i32 v4, v4, 0, v5
	v_lshl_add_u32 v2, v2, 2, s0
	v_med3_i32 v2, v2, 0, v6
	v_lshlrev_b32_e32 v3, 14, v3
	v_lshlrev_b32_e32 v4, 7, v4
	v_or3_b32 v98, v4, v3, v2
	v_min_u32_e32 v2, 3, v48
	v_or_b32_e32 v56, 24, v2
	v_lshrrev_b32_e32 v122, 4, v1
	v_lshl_or_b32 v1, v56, 6, v1
	v_mul_u32_u24_e32 v2, 0x25f, v1
	v_lshrrev_b32_e32 v2, 16, v2
	v_mad_i32_i24 v1, v2, s1, v1
	v_mul_i32_i24_sdwa v3, sext(v1), s6 dst_sel:DWORD dst_unused:UNUSED_PAD src0_sel:WORD_0 src1_sel:DWORD
	v_lshrrev_b32_e32 v4, 31, v3
	v_add_u16_sdwa v3, v3, v4 dst_sel:DWORD dst_unused:UNUSED_PAD src0_sel:WORD_1 src1_sel:DWORD
	v_bfe_i32 v3, v3, 0, 16
	v_mad_i32_i24 v1, v3, s7, v1
	v_add_u32_e32 v3, s25, v3
	v_and_b32_e32 v93, 15, v0
	v_lshrrev_b32_e32 v120, 8, v0
	s_lshl_b32 s18, s24, 18
	v_min_u32_e32 v2, 15, v2
	v_med3_i32 v3, v3, 0, v5
	v_lshl_add_u32 v1, v1, 2, s0
	v_and_b32_e32 v121, 3, v48
	v_med3_i32 v1, v1, 0, v6
	v_lshlrev_b32_e32 v2, 14, v2
	v_lshlrev_b32_e32 v3, 7, v3
	v_lshl_or_b32 v123, v120, 4, v93
	s_movk_i32 s0, 0x42
	s_cmp_lg_u32 0, -1
	v_or3_b32 v100, v3, v2, v1
	v_mad_u32_u24 v1, v121, s0, v123
	s_cselect_b32 s0, 0, 0
	v_lshlrev_b32_e32 v2, 7, v1
	v_bitop3_b32 v3, v1, v122, 7 bitop3:0x6c
	v_add_u32_e32 v1, 33, v1
	s_add_i32 s1, s0, 0xc600
	v_lshl_or_b32 v126, v3, 4, v2
	v_lshlrev_b32_e32 v2, 7, v1
	v_bitop3_b32 v1, v1, v122, 7 bitop3:0x6c
	v_add_u32_e32 v124, s1, v46
	s_add_i32 s1, s0, 0xca00
	v_lshl_or_b32 v127, v1, 4, v2
	v_add_u32_e32 v1, s1, v46
	s_add_i32 s1, s0, 0xce00
	s_waitcnt vmcnt(0)
	s_waitcnt lgkmcnt(0)
	s_barrier
	ds_read_b128 v[42:45], v124
	ds_read_b128 v[38:41], v1
	v_add_u32_e32 v1, s1, v46
	s_add_i32 s1, s0, 0xd200
	ds_read_b128 v[34:37], v1
	v_add_u32_e32 v1, s1, v46
	s_add_i32 s1, s0, 0xd600
	ds_read_b128 v[30:33], v1
	v_add_u32_e32 v1, s1, v46
	s_add_i32 s1, s0, 0xda00
	ds_read_b128 v[26:29], v1
	v_add_u32_e32 v1, s1, v46
	s_add_i32 s1, s0, 0xde00
	ds_read_b128 v[22:25], v1
	v_add_u32_e32 v1, s1, v46
	s_add_i32 s1, s0, 0xe200
	ds_read_b128 v[10:13], v1
	v_add_u32_e32 v1, s1, v46
	s_add_i32 s1, s0, 0xe600
	ds_read_b128 v[6:9], v1
	v_add_u32_e32 v1, s1, v46
	ds_read_b128 v[2:5], v1
	v_add_u32_e32 v1, s0, v126
	ds_read_b128 v[14:17], v1
	v_add_u32_e32 v1, s0, v127
	s_add_i32 s0, s0, 0xea00
	v_add_u32_e32 v125, s0, v46
	s_lshl_b32 s0, s24, 20
	s_add_u32 s10, s2, s0
	v_mov_b32_e32 v95, 0
	v_lshlrev_b32_e32 v0, 4, v0
	ds_read_b128 v[18:21], v1
	s_addc_u32 s11, s3, 0
	v_lshlrev_b32_e32 v91, 10, v47
	v_and_b32_e32 v0, 0x1c00, v0
	v_mov_b32_e32 v1, v95
	v_mov_b32_e32 v47, 0x28800
	s_add_u32 s0, s10, 0x400000
	v_mad_u64_u32 v[54:55], s[2:3], s24, v47, v[0:1]
	s_addc_u32 s1, s11, 0
	v_lshlrev_b32_e32 v48, 2, v94
	v_mov_b32_e32 v49, v95
	v_lshlrev_b32_e32 v50, 2, v96
	v_mov_b32_e32 v51, v95
	v_lshlrev_b32_e32 v52, 2, v98
	v_mov_b32_e32 v53, v95
	v_or_b32_e32 v54, v54, v46
	v_lshlrev_b32_e32 v46, 2, v100
	v_mov_b32_e32 v47, v95
	s_waitcnt lgkmcnt(0)
	v_lshl_add_u64 v[0:1], s[0:1], 0, v[48:49]
	v_lshl_add_u64 v[106:107], s[0:1], 0, v[50:51]
	v_lshl_add_u64 v[110:111], s[0:1], 0, v[52:53]
	v_lshl_add_u64 v[112:113], s[10:11], 0, v[46:47]
	v_lshl_add_u64 v[114:115], s[0:1], 0, v[46:47]
	v_lshl_add_u64 v[46:47], s[20:21], 0, v[54:55]
	s_mov_b64 s[0:1], 0xd000
	v_lshl_add_u64 v[116:117], v[46:47], 0, s[0:1]
	s_movk_i32 s0, 0xc000
	s_movk_i32 s2, 0xe000
	s_mov_b32 s19, 0
	v_accvgpr_write_b32 a3, 0
	v_accvgpr_write_b32 a2, 0
	v_accvgpr_write_b32 a1, 0
	v_accvgpr_write_b32 a0, 0
	v_accvgpr_write_b32 a7, 0
	v_accvgpr_write_b32 a6, 0
	v_accvgpr_write_b32 a5, 0
	v_accvgpr_write_b32 a4, 0
	v_accvgpr_write_b32 a15, 0
	v_accvgpr_write_b32 a14, 0
	v_accvgpr_write_b32 a13, 0
	v_accvgpr_write_b32 a12, 0
	v_accvgpr_write_b32 a19, 0
	v_accvgpr_write_b32 a18, 0
	v_accvgpr_write_b32 a17, 0
	v_accvgpr_write_b32 a16, 0
	v_accvgpr_write_b32 a31, 0
	v_accvgpr_write_b32 a30, 0
	v_accvgpr_write_b32 a29, 0
	v_accvgpr_write_b32 a28, 0
	v_accvgpr_write_b32 a63, 0
	v_accvgpr_write_b32 a62, 0
	v_accvgpr_write_b32 a61, 0
	v_accvgpr_write_b32 a60, 0
	v_accvgpr_write_b32 a11, 0
	v_accvgpr_write_b32 a10, 0
	v_accvgpr_write_b32 a9, 0
	v_accvgpr_write_b32 a8, 0
	v_accvgpr_write_b32 a23, 0
	v_accvgpr_write_b32 a22, 0
	v_accvgpr_write_b32 a21, 0
	v_accvgpr_write_b32 a20, 0
	v_accvgpr_write_b32 a27, 0
	v_accvgpr_write_b32 a26, 0
	v_accvgpr_write_b32 a25, 0
	v_accvgpr_write_b32 a24, 0
	v_accvgpr_write_b32 a39, 0
	v_accvgpr_write_b32 a38, 0
	v_accvgpr_write_b32 a37, 0
	v_accvgpr_write_b32 a36, 0
	v_accvgpr_write_b32 a47, 0
	v_accvgpr_write_b32 a46, 0
	v_accvgpr_write_b32 a45, 0
	v_accvgpr_write_b32 a44, 0
	v_accvgpr_write_b32 a67, 0
	v_accvgpr_write_b32 a66, 0
	v_accvgpr_write_b32 a65, 0
	v_accvgpr_write_b32 a64, 0
	v_accvgpr_write_b32 a35, 0
	v_accvgpr_write_b32 a34, 0
	v_accvgpr_write_b32 a33, 0
	v_accvgpr_write_b32 a32, 0
	v_accvgpr_write_b32 a43, 0
	v_accvgpr_write_b32 a42, 0
	v_accvgpr_write_b32 a41, 0
	v_accvgpr_write_b32 a40, 0
	v_accvgpr_write_b32 a51, 0
	v_accvgpr_write_b32 a50, 0
	v_accvgpr_write_b32 a49, 0
	v_accvgpr_write_b32 a48, 0
	v_accvgpr_write_b32 a55, 0
	v_accvgpr_write_b32 a54, 0
	v_accvgpr_write_b32 a53, 0
	v_accvgpr_write_b32 a52, 0
	v_accvgpr_write_b32 a59, 0
	v_accvgpr_write_b32 a58, 0
	v_accvgpr_write_b32 a57, 0
	v_accvgpr_write_b32 a56, 0
	v_accvgpr_write_b32 a71, 0
	v_accvgpr_write_b32 a70, 0
	v_accvgpr_write_b32 a69, 0
	v_accvgpr_write_b32 a68, 0
	v_lshl_add_u64 v[102:103], s[10:11], 0, v[48:49]
	v_mov_b32_e32 v97, v95
	v_mov_b32_e32 v99, v95
	v_mov_b32_e32 v101, v95
	v_lshlrev_b32_e32 v119, 10, v56
	v_lshl_add_u64 v[104:105], s[10:11], 0, v[50:51]
	v_lshl_add_u64 v[108:109], s[10:11], 0, v[52:53]
	s_mov_b32 s20, 1
	s_mov_b32 s1, -1
	s_mov_b32 s3, -1
	s_add_i32 s17, 0, 0x16000
	s_add_i32 s16, 0, 0x1d000
	s_mov_b64 s[6:7], 0x4800
	v_readfirstlane_b32 s32, v118
	v_readfirstlane_b32 s33, v90
	v_readfirstlane_b32 s34, v92
	s_nop 3
	s_add_i32 s32, s32, 0xc600
	s_add_i32 s33, s33, 0xc600
	s_add_i32 s34, s34, 0xc600
.Lk3_top:
	s_bitcmp1_b32 s19, 0
	s_cselect_b32 s14, 0x4800, 0
	v_add_u32_e32 v78, s14, v125
	v_mfma_f32_16x16x32_f16 a[0:3], v[42:45], v[14:17], a[0:3]
	ds_read_b128 v[70:73], v78
	s_add_i32 s15, s19, 1
	v_mfma_f32_16x16x32_f16 a[4:7], v[42:45], v[18:21], a[4:7]
	ds_read_b128 v[66:69], v78 offset:1024
	s_mul_hi_u32 s28, s15, 0xaaaaaaab
	v_mfma_f32_16x16x32_f16 a[12:15], v[38:41], v[14:17], a[12:15]
	ds_read_b128 v[58:61], v78 offset:2048
	s_lshr_b32 s28, s28, 1
	s_bitcmp1_b32 s15, 0
	s_cselect_b32 s31, 0x4800, 0
	v_mfma_f32_16x16x32_f16 a[16:19], v[38:41], v[18:21], a[16:19]
	ds_read_b128 v[54:57], v78 offset:3072
	s_mul_i32 s29, s28, 3
	v_xor_b32_e32 v82, 64, v126
	v_mfma_f32_16x16x32_f16 a[28:31], v[34:37], v[14:17], a[28:31]
	ds_read_b128 v[46:49], v78 offset:4096
	s_sub_i32 s29, s15, s29
	v_xor_b32_e32 v86, 64, v127
	v_mfma_f32_16x16x32_f16 a[60:63], v[34:37], v[18:21], a[60:63]
	ds_read_b128 v[50:53], v78 offset:5120
	s_add_i32 s30, s29, 1
	v_add_lshl_u32 v128, s28, v121, 1
	v_mfma_f32_16x16x32_f16 a[8:11], v[30:33], v[14:17], a[8:11]
	ds_read_b128 v[62:65], v78 offset:6144
	v_and_or_b32 v129, s29, 1, v128
	v_mfma_f32_16x16x32_f16 a[20:23], v[30:33], v[18:21], a[20:23]
	ds_read_b128 v[74:77], v78 offset:7168
	v_and_or_b32 v130, s30, 1, v128
	s_lshr_b32 s29, s29, 1
	s_lshr_b32 s30, s30, 1
	v_mfma_f32_16x16x32_f16 a[24:27], v[26:29], v[14:17], a[24:27]
	ds_read_b128 v[78:81], v78 offset:8192
	v_lshl_add_u32 v129, v129, 5, v129
	v_mfma_f32_16x16x32_f16 a[36:39], v[26:29], v[18:21], a[36:39]
	ds_read_b128 v[82:85], v82
	v_lshl_add_u32 v130, v130, 5, v130
	v_mfma_f32_16x16x32_f16 a[44:47], v[22:25], v[14:17], a[44:47]
	ds_read_b128 v[86:89], v86
	v_add3_u32 v129, v123, s29, v129
	v_mfma_f32_16x16x32_f16 a[64:67], v[22:25], v[18:21], a[64:67]
	v_add3_u32 v130, v123, s30, v130
	v_lshlrev_b32_e32 v128, 7, v129
	v_mfma_f32_16x16x32_f16 a[32:35], v[10:13], v[14:17], a[32:35]
	v_bitop3_b32 v129, v129, v122, 7 bitop3:0x6c
	v_lshlrev_b32_e32 v136, 7, v130
	v_mfma_f32_16x16x32_f16 a[40:43], v[10:13], v[18:21], a[40:43]
	v_bitop3_b32 v130, v130, v122, 7 bitop3:0x6c
	v_lshl_or_b32 v126, v129, 4, v128
	v_mfma_f32_16x16x32_f16 a[48:51], v[6:9], v[14:17], a[48:51]
	v_lshl_or_b32 v127, v130, 4, v136
	v_add_u32_e32 v131, s31, v124
	v_mfma_f32_16x16x32_f16 a[52:55], v[6:9], v[18:21], a[52:55]
	v_lshl_add_u64 v[132:133], v[116:117], 0, s[0:1]
	s_add_i32 s35, s32, s14
	v_mfma_f32_16x16x32_f16 a[56:59], v[2:5], v[14:17], a[56:59]
	v_lshl_add_u64 v[134:135], v[116:117], 0, s[2:3]
	s_add_i32 s36, s33, s14
	s_add_i32 s37, s34, s14
	v_mfma_f32_16x16x32_f16 a[68:71], v[2:5], v[18:21], a[68:71]
	s_cmp_eq_u32 s19, 8
	s_waitcnt lgkmcnt(0)
	s_cbranch_scc1 .Lk3_nb
	s_waitcnt vmcnt(0)
.Lk3_nb:
	s_barrier
	s_cmp_gt_u32 s19, 6
	s_cbranch_scc1 .Lk3_nodma
	s_mov_b32 m0, s35
	s_nop 0
	global_load_lds_dwordx4 v[132:133], off
	s_mov_b32 m0, s36
	s_nop 0
	global_load_lds_dwordx4 v[134:135], off
	s_cmp_lt_u32 s34, 0x10e00
	s_cbranch_scc0 .Lk3_nodma
	s_mov_b32 m0, s37
	s_nop 0
	global_load_lds_dwordx4 v[116:117], off

.Lk3_h2:
	v_mfma_f32_16x16x32_f16 a[0:3], v[70:73], v[82:85], a[0:3]
	ds_read_b128 v[42:45], v131
	v_mfma_f32_16x16x32_f16 a[4:7], v[70:73], v[86:89], a[4:7]
	ds_read_b128 v[38:41], v131 offset:1024
	v_mfma_f32_16x16x32_f16 a[12:15], v[66:69], v[82:85], a[12:15]
	ds_read_b128 v[34:37], v131 offset:2048
	v_mfma_f32_16x16x32_f16 a[16:19], v[66:69], v[86:89], a[16:19]
	ds_read_b128 v[30:33], v131 offset:3072
	v_mfma_f32_16x16x32_f16 a[28:31], v[58:61], v[82:85], a[28:31]
	ds_read_b128 v[26:29], v131 offset:4096
	v_mfma_f32_16x16x32_f16 a[60:63], v[58:61], v[86:89], a[60:63]
	ds_read_b128 v[22:25], v131 offset:5120
	v_mfma_f32_16x16x32_f16 a[8:11], v[54:57], v[82:85], a[8:11]
	ds_read_b128 v[10:13], v131 offset:6144
	v_mfma_f32_16x16x32_f16 a[20:23], v[54:57], v[86:89], a[20:23]
	ds_read_b128 v[6:9], v131 offset:7168
	v_mfma_f32_16x16x32_f16 a[24:27], v[46:49], v[82:85], a[24:27]
	ds_read_b128 v[2:5], v131 offset:8192
	v_mfma_f32_16x16x32_f16 a[36:39], v[46:49], v[86:89], a[36:39]
	ds_read_b128 v[14:17], v126
	v_mfma_f32_16x16x32_f16 a[44:47], v[50:53], v[82:85], a[44:47]
	ds_read_b128 v[18:21], v127
	v_mfma_f32_16x16x32_f16 a[64:67], v[50:53], v[86:89], a[64:67]
	v_mfma_f32_16x16x32_f16 a[32:35], v[62:65], v[82:85], a[32:35]
	v_mfma_f32_16x16x32_f16 a[40:43], v[62:65], v[86:89], a[40:43]
	v_mfma_f32_16x16x32_f16 a[48:51], v[74:77], v[82:85], a[48:51]
	v_mfma_f32_16x16x32_f16 a[52:55], v[74:77], v[86:89], a[52:55]
	v_mfma_f32_16x16x32_f16 a[56:59], v[78:81], v[82:85], a[56:59]
	v_mfma_f32_16x16x32_f16 a[68:71], v[78:81], v[86:89], a[68:71]
	s_waitcnt lgkmcnt(0)
	v_lshl_add_u64 v[116:117], v[116:117], 0, s[6:7]
	s_mov_b32 s19, s15
	s_cmp_eq_u32 s15, 9
	s_cbranch_scc0 .Lk3_top

	.amdhsa_kernel _Z7kfinal3PKDF16_PKfS2_S2_PK15HIP_vector_typeIjLj4EES2_Pf
		.amdhsa_group_segment_fixed_size 0
		.amdhsa_private_segment_fixed_size 0
		.amdhsa_kernarg_size 56
		.amdhsa_user_sgpr_count 2
		.amdhsa_user_sgpr_dispatch_ptr 0
		.amdhsa_user_sgpr_queue_ptr 0
		.amdhsa_user_sgpr_kernarg_segment_ptr 1
		.amdhsa_user_sgpr_dispatch_id 0
		.amdhsa_user_sgpr_kernarg_preload_length 0
		.amdhsa_user_sgpr_kernarg_preload_offset 0
		.amdhsa_user_sgpr_private_segment_size 0
		.amdhsa_uses_dynamic_stack 0
		.amdhsa_enable_private_segment 0
		.amdhsa_system_sgpr_workgroup_id_x 1
		.amdhsa_system_sgpr_workgroup_id_y 0
		.amdhsa_system_sgpr_workgroup_id_z 0
		.amdhsa_system_sgpr_workgroup_info 0
		.amdhsa_system_vgpr_workitem_id 0
		.amdhsa_next_free_vgpr 213
		.amdhsa_next_free_sgpr 38
		.amdhsa_accum_offset 140
		.amdhsa_reserve_vcc 1
		.amdhsa_float_round_mode_32 0
		.amdhsa_float_round_mode_16_64 0
		.amdhsa_float_denorm_mode_32 3
		.amdhsa_float_denorm_mode_16_64 3
		.amdhsa_dx10_clamp 1
		.amdhsa_ieee_mode 1
		.amdhsa_fp16_overflow 0
		.amdhsa_tg_split 0
		.amdhsa_exception_fp_ieee_invalid_op 0
		.amdhsa_exception_fp_denorm_src 0
		.amdhsa_exception_fp_ieee_div_zero 0
		.amdhsa_exception_fp_ieee_overflow 0
		.amdhsa_exception_fp_ieee_underflow 0
		.amdhsa_exception_fp_ieee_inexact 0
		.amdhsa_exception_int_div_zero 0
	.end_amdhsa_kernel

amdhsa.kernels:
  - .agpr_count:     0
    .args:
      - .actual_access:  read_only
        .address_space:  global
        .offset:         0
        .size:           8
        .value_kind:     global_buffer
      - .actual_access:  read_only
        .address_space:  global
        .offset:         8
        .size:           8
        .value_kind:     global_buffer
      - .actual_access:  read_only
        .address_space:  global
        .offset:         16
        .size:           8
        .value_kind:     global_buffer
      - .actual_access:  read_only
        .address_space:  global
        .offset:         24
        .size:           8
        .value_kind:     global_buffer
      - .actual_access:  read_only
        .address_space:  global
        .offset:         32
        .size:           8
        .value_kind:     global_buffer
      - .actual_access:  read_only
        .address_space:  global
        .offset:         40
        .size:           8
        .value_kind:     global_buffer
      - .actual_access:  write_only
        .address_space:  global
        .offset:         48
        .size:           8
        .value_kind:     global_buffer
      - .actual_access:  write_only
        .address_space:  global
        .offset:         56
        .size:           8
        .value_kind:     global_buffer
      - .actual_access:  write_only
        .address_space:  global
        .offset:         64
        .size:           8
        .value_kind:     global_buffer
      - .actual_access:  write_only
        .address_space:  global
        .offset:         72
        .size:           8
        .value_kind:     global_buffer
    .group_segment_fixed_size: 12000
    .kernarg_segment_align: 8
    .kernarg_segment_size: 80
    .language:       OpenCL C
    .language_version:
      - 2
      - 0
    .max_flat_workgroup_size: 256
    .name:           _Z2k0PKfS0_S0_S0_S0_S0_PDF16_PfS1_S1_
    .private_segment_fixed_size: 0
    .sgpr_count:     24
    .sgpr_spill_count: 0
    .symbol:         _Z2k0PKfS0_S0_S0_S0_S0_PDF16_PfS1_S1_.kd
    .uniform_work_group_size: 1
    .uses_dynamic_stack: false
    .vgpr_count:     150
    .vgpr_spill_count: 0
    .wavefront_size: 64
  - .agpr_count:     16
    .args:
      - .actual_access:  read_only
        .address_space:  global
        .offset:         0
        .size:           8
        .value_kind:     global_buffer
      - .actual_access:  read_only
        .address_space:  global
        .offset:         8
        .size:           8
        .value_kind:     global_buffer
      - .actual_access:  read_only
        .address_space:  global
        .offset:         16
        .size:           8
        .value_kind:     global_buffer
      - .actual_access:  read_only
        .address_space:  global
        .offset:         24
        .size:           8
        .value_kind:     global_buffer
      - .actual_access:  read_only
        .address_space:  global
        .offset:         32
        .size:           8
        .value_kind:     global_buffer
      - .actual_access:  write_only
        .address_space:  global
        .offset:         40
        .size:           8
        .value_kind:     global_buffer
      - .actual_access:  write_only
        .address_space:  global
        .offset:         48
        .size:           8
        .value_kind:     global_buffer
    .group_segment_fixed_size: 14112
    .kernarg_segment_align: 8
    .kernarg_segment_size: 56
    .language:       OpenCL C
    .language_version:
      - 2
      - 0
    .max_flat_workgroup_size: 256
    .name:           _Z4khidPKDF16_PKfS2_S2_S0_PDF16_Pf
    .private_segment_fixed_size: 0
    .sgpr_count:     24
    .sgpr_spill_count: 0
    .symbol:         _Z4khidPKDF16_PKfS2_S2_S0_PDF16_Pf.kd
    .uniform_work_group_size: 1
    .uses_dynamic_stack: false
    .vgpr_count:     148
    .vgpr_spill_count: 0
    .wavefront_size: 64
  - .agpr_count:     144
    .args:
      - .actual_access:  read_only
        .address_space:  global
        .offset:         0
        .size:           8
        .value_kind:     global_buffer
      - .actual_access:  read_only
        .address_space:  global
        .offset:         8
        .size:           8
        .value_kind:     global_buffer
      - .actual_access:  read_only
        .address_space:  global
        .offset:         16
        .size:           8
        .value_kind:     global_buffer
      - .actual_access:  read_only
        .address_space:  global
        .offset:         24
        .size:           8
        .value_kind:     global_buffer
      - .address_space:  global
        .offset:         32
        .size:           8
        .value_kind:     global_buffer
      - .address_space:  global
        .offset:         40
        .size:           8
        .value_kind:     global_buffer
      - .address_space:  global
        .offset:         48
        .size:           8
        .value_kind:     global_buffer
    .group_segment_fixed_size: 0
    .kernarg_segment_align: 8
    .kernarg_segment_size: 56
    .language:       OpenCL C
    .language_version:
      - 2
      - 0
    .max_flat_workgroup_size: 256
    .name:           _Z6kfinalPKDF16_PKfS2_S2_PK15HIP_vector_typeIjLj4EES2_Pf
    .private_segment_fixed_size: 0
    .sgpr_count:     41
    .sgpr_spill_count: 0
    .symbol:         _Z6kfinalPKDF16_PKfS2_S2_PK15HIP_vector_typeIjLj4EES2_Pf.kd
    .uniform_work_group_size: 1
    .uses_dynamic_stack: false
    .vgpr_count:     400
    .vgpr_spill_count: 0
    .wavefront_size: 64
  - .agpr_count:     73
    .args:
      - .actual_access:  read_only
        .address_space:  global
        .offset:         0
        .size:           8
        .value_kind:     global_buffer
      - .actual_access:  read_only
        .address_space:  global
        .offset:         8
        .size:           8
        .value_kind:     global_buffer
      - .actual_access:  read_only
        .address_space:  global
        .offset:         16
        .size:           8
        .value_kind:     global_buffer
      - .actual_access:  read_only
        .address_space:  global
        .offset:         24
        .size:           8
        .value_kind:     global_buffer
      - .address_space:  global
        .offset:         32
        .size:           8
        .value_kind:     global_buffer
      - .address_space:  global
        .offset:         40
        .size:           8
        .value_kind:     global_buffer
      - .address_space:  global
        .offset:         48
        .size:           8
        .value_kind:     global_buffer
    .group_segment_fixed_size: 0
    .kernarg_segment_align: 8
    .kernarg_segment_size: 56
    .language:       OpenCL C
    .language_version:
      - 2
      - 0
    .max_flat_workgroup_size: 512
    .name:           _Z7kfinal3PKDF16_PKfS2_S2_PK15HIP_vector_typeIjLj4EES2_Pf
    .private_segment_fixed_size: 0
    .sgpr_count:     44
    .sgpr_spill_count: 0
    .symbol:         _Z7kfinal3PKDF16_PKfS2_S2_PK15HIP_vector_typeIjLj4EES2_Pf.kd
    .uniform_work_group_size: 1
    .uses_dynamic_stack: false
    .vgpr_count:     213
    .vgpr_spill_count: 0
    .wavefront_size: 64
